# first grid barrier: census of the 16 per-XCD counters issued as one batch of loads instead of 16 serialized round trips
# baseline (speedup 1.0000x reference)
; DI unsigned xb_ld(unsigned* p)              { return __hip_atomic_load(p, __ATOMIC_RELAXED, __HIP_MEMORY_SCOPE_AGENT); }
; DI void xcd_barrier_complete(unsigned* bar, unsigned x, unsigned& nloc, unsigned& nx) {
;     ...
;     for (;;) {
;         sum = 0u; cnt = 0u; mine = 0u;
; #pragma unroll
;         for (unsigned j = 0; j < 16; ++j) { const unsigned c = xb_ld(&bar[XB_XCNT(j)]); sum += c; cnt += (c > 0u) ? 1u : 0u; mine = (j == x) ? c : mine; }
;         if (sum == G) break;
;         __builtin_amdgcn_s_sleep(1);
;         if ((++sp & 255u) == 0u) { if (xb_ld(&bar[XB_TMO])) break; if (sp > XB_SPIN_CAP) { atomicAdd(&bar[XB_TMO], 1u); break; } }
;     }
.LBB0_59:
	v_readlane_b32 s28, v252, 7
	v_readlane_b32 s29, v252, 8
	v_readlane_b32 s30, v252, 9
	v_readlane_b32 s31, v252, 10
	v_readlane_b32 s32, v252, 11
	v_readlane_b32 s33, v252, 12
	v_readlane_b32 s34, v252, 13
	v_readlane_b32 s35, v252, 14
	v_readlane_b32 s36, v252, 15
	v_readlane_b32 s37, v252, 16
	v_readlane_b32 s38, v252, 17
	v_readlane_b32 s39, v252, 18
	v_readlane_b32 s40, v252, 19
	v_readlane_b32 s41, v252, 20
	v_readlane_b32 s76, v252, 21
	v_readlane_b32 s77, v252, 22
	v_readlane_b32 s78, v252, 23
	v_readlane_b32 s79, v252, 24
	v_readlane_b32 s80, v252, 25
	v_readlane_b32 s81, v252, 26
	v_readlane_b32 s82, v252, 27
	v_readlane_b32 s83, v252, 28
	v_readlane_b32 s84, v252, 29
	v_readlane_b32 s85, v252, 30
	v_readlane_b32 s86, v252, 31
	v_readlane_b32 s87, v252, 32
	v_readlane_b32 s88, v252, 33
	v_readlane_b32 s89, v252, 34
	s_mov_b64 s[6:7], -1
	s_nop 4
	global_load_dword v1, v16, s[50:51] sc1
	global_load_dword v0, v16, s[46:47] sc1
	global_load_dword v2, v16, s[28:29] sc1
	global_load_dword v3, v16, s[30:31] sc1
	global_load_dword v4, v16, s[32:33] sc1
	global_load_dword v5, v16, s[34:35] sc1
	global_load_dword v6, v16, s[36:37] sc1
	global_load_dword v7, v16, s[38:39] sc1
	global_load_dword v8, v16, s[40:41] sc1
	global_load_dword v9, v16, s[76:77] sc1
	global_load_dword v10, v16, s[78:79] sc1
	global_load_dword v11, v16, s[80:81] sc1
	global_load_dword v12, v16, s[82:83] sc1
	global_load_dword v13, v16, s[84:85] sc1
	global_load_dword v14, v16, s[86:87] sc1
	global_load_dword v15, v16, s[88:89] sc1
	s_mov_b64 s[4:5], -1
	s_waitcnt vmcnt(0)
	v_add_u32_e32 v17, v0, v1
	v_add_u32_e32 v17, v17, v2
	v_add_u32_e32 v17, v17, v3
	v_add_u32_e32 v17, v17, v4
	v_add_u32_e32 v17, v17, v5
	v_add_u32_e32 v17, v17, v6
	v_add_u32_e32 v17, v17, v7
	v_add_u32_e32 v17, v17, v8
	v_add_u32_e32 v17, v17, v9
	v_add_u32_e32 v17, v17, v10
	v_add_u32_e32 v17, v17, v11
	v_add_u32_e32 v17, v17, v12
	v_add_u32_e32 v17, v17, v13
	v_add_u32_e32 v17, v17, v14
	v_add_u32_e32 v17, v17, v15
	v_cmp_eq_u32_e32 vcc, s3, v17
	s_cbranch_vccnz .LBB0_58
	s_and_b32 s4, s2, 0xff
	s_cmp_eq_u32 s4, 0
	s_mov_b64 s[4:5], -1
	s_mov_b64 s[8:9], -1
	s_sleep 1
	s_cbranch_scc0 .LBB0_63
	v_readlane_b32 s4, v252, 5
	v_readlane_b32 s5, v252, 6
	s_nop 4
	global_load_dword v17, v16, s[4:5] sc1
	s_waitcnt vmcnt(0)
	v_cmp_eq_u32_e32 vcc, 0, v17
	s_cbranch_vccnz .LBB0_65
	s_mov_b64 s[8:9], 0
	s_mov_b64 s[4:5], -1
